# FIN row sum of squares: the five LDS swizzle steps replaced by four DPP adds and a permlane16 swap
# baseline (speedup 1.0000x reference)
; __device__ __forceinline__ float wave_sum(float v) {
;     v = xor_add<1>(v); v = xor_add<2>(v); v = xor_add<4>(v); v = xor_add<8>(v); v = xor_add<16>(v); v = xor_add<32>(v);
;     return v;
; }
; template <int PH, bool PRB = false>
; __device__ __forceinline__ void run_phase(int layer, LAS unsigned char* lds, const int wv_) {
;     ...
;             u32x2 cc[2][4]; unsigned aa[2][4], bb[2][4];
; #pragma unroll
;             for (int q = 0; q < 2; ++q) { const int r = r0 + q * NGW < S ? r0 + q * NGW : r0;
;                 const u32x2* hr = (const u32x2*)(hb + (size_t)r * D); const unsigned* y0 = (const unsigned*)((const unsigned char*)ys + (size_t)(2 * r) * D); const unsigned* y1 = (const unsigned*)((const unsigned char*)ys + (size_t)(2 * r + 1) * D);
; #pragma unroll
;                 for (int j = 0; j < 4; ++j) { cc[q][j] = hr[lane + 64 * j]; aa[q][j] = y0[lane + 64 * j]; bb[q][j] = y1[lane + 64 * j]; } }
; #pragma unroll
;             for (int q = 0; q < 2; ++q) { const int r = r0 + q * NGW; if (r < S) {
;                 float4 v[4]; float ss = 0.f;
; #pragma unroll
;                 for (int j = 0; j < 4; ++j) {
;                     typedef float f2_ __attribute__((ext_vector_type(2)));
;                     const u32x2 c = cc[q][j]; const f2_ a0 = __builtin_amdgcn_cvt_pk_f32_fp8((int)aa[q][j], false), a1 = __builtin_amdgcn_cvt_pk_f32_fp8((int)aa[q][j], true), b0 = __builtin_amdgcn_cvt_pk_f32_fp8((int)bb[q][j], false), b1 = __builtin_amdgcn_cvt_pk_f32_fp8((int)bb[q][j], true);
;                     constexpr float iy = 1.0f / pg8::YS8_SCALE;
;                     v[j].x = __uint_as_float(c.x << 16) + (a0[0] + b0[0]) * iy; v[j].y = __uint_as_float(c.x & 0xffff0000u) + (a0[1] + b0[1]) * iy;
;                     v[j].z = __uint_as_float(c.y << 16) + (a1[0] + b1[0]) * iy; v[j].w = __uint_as_float(c.y & 0xffff0000u) + (a1[1] + b1[1]) * iy;
;                     ss += v[j].x * v[j].x + v[j].y * v[j].y + v[j].z * v[j].z + v[j].w * v[j].w;
;                 }
;                 ss = wave_sum(ss);
.LBB0_1762:
	s_add_i32 s3, s90, s2
	s_cmpk_lt_i32 s3, 0x4000
	s_cselect_b64 s[18:19], -1, 0
	v_lshl_add_u64 v[56:57], s[10:11], 0, v[20:21]
	s_and_b64 s[8:9], s[18:19], exec
	v_add_co_u32_e32 v32, vcc, s29, v56
	s_cselect_b32 s8, s3, s2
	s_ashr_i32 s13, s12, 31
	v_addc_co_u32_e32 v33, vcc, 0, v57, vcc
	s_lshl_b64 s[20:21], s[12:13], 10
	global_load_dwordx2 v[40:41], v[32:33], off
	global_load_dwordx2 v[42:43], v[32:33], off offset:1024
	global_load_dwordx2 v[50:51], v[32:33], off offset:1536
	global_load_dwordx2 v[44:45], v[32:33], off offset:512
	v_lshl_add_u64 v[32:33], v[18:19], 0, s[20:21]
	s_add_i32 s20, s12, 1
	s_ashr_i32 s21, s20, 31
	global_load_dword v92, v[32:33], off offset:768
	global_load_dword v52, v[32:33], off offset:256
	global_load_dword v72, v[32:33], off offset:512
	s_lshl_b64 s[20:21], s[20:21], 10
	global_load_dword v78, v[32:33], off
	v_lshl_add_u64 v[32:33], v[18:19], 0, s[20:21]
	global_load_dword v82, v[32:33], off
	global_load_dword v86, v[32:33], off offset:256
	global_load_dword v90, v[32:33], off offset:512
	global_load_dword v93, v[32:33], off offset:768
	s_lshl_b32 s20, s8, 1
	s_ashr_i32 s9, s8, 31
	s_ashr_i32 s21, s20, 31
	s_or_b32 s26, s20, 1
	s_lshl_b64 s[8:9], s[8:9], 11
	s_lshl_b64 s[20:21], s[20:21], 10
	s_ashr_i32 s27, s26, 31
	v_lshl_add_u64 v[32:33], v[16:17], 0, s[8:9]
	s_lshl_b64 s[8:9], s[26:27], 10
	v_lshl_add_u64 v[46:47], v[18:19], 0, s[20:21]
	global_load_dwordx2 v[38:39], v[32:33], off
	global_load_dwordx2 v[36:37], v[32:33], off offset:512
	global_load_dwordx2 v[34:35], v[32:33], off offset:1024
	s_nop 0
	global_load_dwordx2 v[32:33], v[32:33], off offset:1536
	v_lshl_add_u64 v[48:49], v[18:19], 0, s[8:9]
	global_load_dword v66, v[46:47], off
	global_load_dword v62, v[46:47], off offset:256
	global_load_dword v60, v[46:47], off offset:512
	global_load_dword v67, v[48:49], off
	global_load_dword v63, v[48:49], off offset:256
	global_load_dword v61, v[48:49], off offset:512
	global_load_dword v58, v[48:49], off offset:768
	global_load_dword v59, v[46:47], off offset:768
	s_mov_b64 s[20:21], -1
	s_and_b64 vcc, exec, s[0:1]
	s_waitcnt vmcnt(23)
	v_lshlrev_b32_e32 v46, 16, v40
	s_waitcnt vmcnt(22)
	v_lshlrev_b32_e32 v68, 16, v42
	v_and_b32_e32 v69, 0xffff0000, v42
	v_lshlrev_b32_e32 v70, 16, v43
	v_and_b32_e32 v71, 0xffff0000, v43
	v_and_b32_e32 v47, 0xffff0000, v40
	s_waitcnt vmcnt(18)
	v_cvt_pk_f32_fp8_e32 v[42:43], v52
	s_waitcnt vmcnt(17)
	v_cvt_pk_f32_fp8_e32 v[54:55], v72
	s_waitcnt vmcnt(15)
	v_cvt_pk_f32_fp8_e32 v[80:81], v82
	v_cvt_pk_f32_fp8_e32 v[76:77], v78
	s_waitcnt vmcnt(14)
	v_cvt_pk_f32_fp8_e32 v[84:85], v86
	v_cvt_pk_f32_fp8_sdwa v[78:79], v78 src0_sel:WORD_1
	v_cvt_pk_f32_fp8_sdwa v[82:83], v82 src0_sel:WORD_1
	s_waitcnt vmcnt(13)
	v_cvt_pk_f32_fp8_e32 v[88:89], v90
	v_cvt_pk_f32_fp8_sdwa v[52:53], v52 src0_sel:WORD_1
	v_cvt_pk_f32_fp8_sdwa v[72:73], v72 src0_sel:WORD_1
	v_cvt_pk_f32_fp8_sdwa v[86:87], v86 src0_sel:WORD_1
	v_cvt_pk_f32_fp8_sdwa v[90:91], v90 src0_sel:WORD_1
	v_lshlrev_b32_e32 v48, 16, v44
	v_and_b32_e32 v49, 0xffff0000, v44
	v_pk_add_f32 v[76:77], v[76:77], v[80:81]
	v_pk_add_f32 v[42:43], v[42:43], v[84:85]
	v_cvt_pk_f32_fp8_e32 v[74:75], v92
	v_pk_add_f32 v[78:79], v[78:79], v[82:83]
	v_pk_add_f32 v[82:83], v[54:55], v[88:89]
	v_pk_fma_f32 v[54:55], v[76:77], 0.5, v[46:47] op_sel_hi:[1,0,1]
	v_pk_fma_f32 v[46:47], v[42:43], 0.5, v[48:49] op_sel_hi:[1,0,1]
	s_waitcnt vmcnt(12)
	v_cvt_pk_f32_fp8_e32 v[48:49], v93
	v_lshlrev_b32_e32 v40, 16, v41
	v_and_b32_e32 v41, 0xffff0000, v41
	v_lshlrev_b32_e32 v44, 16, v45
	v_and_b32_e32 v45, 0xffff0000, v45
	v_pk_add_f32 v[80:81], v[52:53], v[86:87]
	v_pk_add_f32 v[72:73], v[72:73], v[90:91]
	v_pk_fma_f32 v[42:43], v[82:83], 0.5, v[68:69] op_sel_hi:[1,0,1]
	v_cvt_pk_f32_fp8_sdwa v[82:83], v92 src0_sel:WORD_1
	v_cvt_pk_f32_fp8_sdwa v[84:85], v93 src0_sel:WORD_1
	v_pk_fma_f32 v[52:53], v[78:79], 0.5, v[40:41] op_sel_hi:[1,0,1]
	v_pk_fma_f32 v[44:45], v[80:81], 0.5, v[44:45] op_sel_hi:[1,0,1]
	v_pk_fma_f32 v[40:41], v[72:73], 0.5, v[70:71] op_sel_hi:[1,0,1]
	v_pk_mul_f32 v[68:69], v[54:55], v[54:55]
	v_pk_mul_f32 v[72:73], v[46:47], v[46:47]
	v_pk_mul_f32 v[70:71], v[52:53], v[52:53]
	v_pk_mul_f32 v[76:77], v[44:45], v[44:45]
	v_pk_mul_f32 v[78:79], v[42:43], v[42:43]
	v_add_f32_e32 v72, v72, v73
	v_add_f32_e32 v68, v68, v69
	v_pk_mul_f32 v[80:81], v[40:41], v[40:41]
	v_lshlrev_b32_e32 v86, 16, v50
	v_and_b32_e32 v87, 0xffff0000, v50
	v_pk_add_f32 v[48:49], v[74:75], v[48:49]
	v_add_f32_e32 v72, v72, v76
	v_add_f32_e32 v68, v68, v70
	v_add_f32_e32 v69, v78, v79
	v_pk_fma_f32 v[48:49], v[48:49], 0.5, v[86:87] op_sel_hi:[1,0,1]
	v_lshlrev_b32_e32 v50, 16, v51
	v_and_b32_e32 v51, 0xffff0000, v51
	v_pk_add_f32 v[74:75], v[82:83], v[84:85]
	v_add_f32_e32 v72, v77, v72
	v_add_f32_e32 v68, v71, v68
	v_add_f32_e32 v69, v69, v80
	v_pk_fma_f32 v[50:51], v[74:75], 0.5, v[50:51] op_sel_hi:[1,0,1]
	v_pk_mul_f32 v[74:75], v[48:49], v[48:49]
	v_add_f32_e32 v68, v68, v72
	v_add_f32_e32 v69, v81, v69
	v_pk_mul_f32 v[82:83], v[50:51], v[50:51]
	v_add_f32_e32 v68, v68, v69
	v_add_f32_e32 v69, v74, v75
	v_add_f32_e32 v69, v69, v82
	v_add_f32_e32 v69, v83, v69
	v_add_f32_e32 v68, v68, v69
	s_nop 1
	s_waitcnt lgkmcnt(0)
	v_add_f32_dpp v68, v68, v68 quad_perm:[1,0,3,2] row_mask:0xf bank_mask:0xf
	s_nop 1
	s_waitcnt lgkmcnt(0)
	v_add_f32_dpp v68, v68, v68 quad_perm:[2,3,0,1] row_mask:0xf bank_mask:0xf
	s_nop 1
	s_waitcnt lgkmcnt(0)
	v_add_f32_dpp v68, v68, v68 row_half_mirror row_mask:0xf bank_mask:0xf
	s_nop 1
	s_waitcnt lgkmcnt(0)
	v_add_f32_dpp v68, v68, v68 row_mirror row_mask:0xf bank_mask:0xf
	v_mov_b32_e32 v69, v68
	s_nop 1
	v_permlane16_swap_b32_e32 v68, v69
	s_waitcnt lgkmcnt(0)
	v_add_f32_e32 v68, v68, v69
	v_mov_b32_e32 v69, v68
	s_nop 1
	v_permlane32_swap_b32_e32 v68, v69
	v_add_f32_e32 v70, v68, v69
	v_fmamk_f32 v68, v70, 0x3a800000, v218
	v_cmp_gt_f32_e64 s[8:9], s61, v68
	v_mul_f32_e32 v69, 0x4b800000, v68
	s_cbranch_vccz .LBB0_1769
; template <int PH, bool PRB = false>
; __device__ __forceinline__ void run_phase(int layer, LAS unsigned char* lds, const int wv_) {
;     ...
;                 } else {
;                     rms_row_bf16(v, 1.0f, nullptr, hbo + (size_t)r * D, lane);
;                     if (!PRB) {
;                         const float rs8 = rsqrtf(ss * (1.0f / D) + 1e-6f); unsigned char* h8 = ws + WS_H + 32 * MiB + (size_t)r * D;
; #pragma unroll
;                         for (int j = 0; j < 4; ++j) { int w = __builtin_amdgcn_cvt_pk_fp8_f32(v[j].x * rs8, v[j].y * rs8, 0, false); w = __builtin_amdgcn_cvt_pk_fp8_f32(v[j].z * rs8, v[j].w * rs8, w, true); ((int*)h8)[lane + 64 * j] = w; }
;                     }
;                     if (lane < 16) sso[(size_t)r * 16 + lane] = lane == 0 ? ss : 0.f;
;                     if (lane == 0 && !PRB) ((float*)(ws + WS_MISC + MISC_RSROW))[r] = rsqrtf(ss * (1.0f / D) + 1e-6f);
	s_mov_b64 s[20:21], 0x4100000
	v_lshl_add_u64 v[72:73], v[56:57], 0, s[20:21]
	s_mov_b64 s[20:21], 0x4100600
	v_lshl_add_u64 v[74:75], v[56:57], 0, s[20:21]
	s_mov_b64 s[20:21], 0x4100400
	v_lshl_add_u64 v[76:77], v[56:57], 0, s[20:21]
	s_mov_b64 s[20:21], 0x4100200
	v_lshl_add_u64 v[56:57], v[56:57], 0, s[20:21]
	v_cvt_pk_bf16_f32 v78, v54, v55
	v_cvt_pk_bf16_f32 v79, v52, v53
	global_store_dwordx2 v[72:73], v[78:79], off
	v_cvt_pk_bf16_f32 v72, v46, v47
	v_cvt_pk_bf16_f32 v73, v44, v45
	global_store_dwordx2 v[56:57], v[72:73], off
	v_cvt_pk_bf16_f32 v56, v42, v43
	v_cvt_pk_bf16_f32 v57, v40, v41
	global_store_dwordx2 v[76:77], v[56:57], off
	v_cvt_pk_bf16_f32 v56, v48, v49
	v_cvt_pk_bf16_f32 v57, v50, v51
	global_store_dwordx2 v[74:75], v[56:57], off
	v_cndmask_b32_e64 v56, v68, v69, s[8:9]
	v_rsq_f32_e32 v56, v56
	v_mov_b32_e32 v74, v65
	v_lshl_add_u64 v[72:73], s[10:11], 0, v[30:31]
	s_mov_b32 s3, 0x2100000
	v_mul_f32_e32 v57, 0x45800000, v56
	v_cndmask_b32_e64 v56, v56, v57, s[8:9]
	v_mul_f32_e32 v57, v54, v56
	v_mul_f32_e32 v71, v55, v56
	v_cvt_pk_fp8_f32 v74, v57, v71
	v_mul_f32_e32 v57, v52, v56
	v_mul_f32_e32 v71, v53, v56
	v_add_co_u32_e32 v72, vcc, s3, v72
	v_cvt_pk_fp8_f32 v74, v57, v71 op_sel:[0,0,1]
	s_nop 0
	v_addc_co_u32_e32 v73, vcc, 0, v73, vcc
	v_mul_f32_e32 v57, v46, v56
	global_store_dword v[72:73], v74, off
	v_mul_f32_e32 v71, v47, v56
	v_mov_b32_e32 v74, v65
	v_cvt_pk_fp8_f32 v74, v57, v71
	v_mul_f32_e32 v57, v44, v56
	v_mul_f32_e32 v71, v45, v56
	v_cvt_pk_fp8_f32 v74, v57, v71 op_sel:[0,0,1]
	v_mul_f32_e32 v57, v42, v56
	v_mul_f32_e32 v71, v43, v56
	global_store_dword v[72:73], v74, off offset:256
	v_mov_b32_e32 v74, v65
	v_cvt_pk_fp8_f32 v74, v57, v71
	v_mul_f32_e32 v57, v40, v56
	v_mul_f32_e32 v71, v41, v56
	v_cvt_pk_fp8_f32 v74, v57, v71 op_sel:[0,0,1]
	v_mul_f32_e32 v57, v48, v56
	v_mul_f32_e32 v71, v49, v56
	global_store_dword v[72:73], v74, off offset:512
	v_mov_b32_e32 v74, v65
	v_cvt_pk_fp8_f32 v74, v57, v71
	v_mul_f32_e32 v57, v50, v56
	v_mul_f32_e32 v71, v51, v56
	v_cvt_pk_fp8_f32 v74, v57, v71 op_sel:[0,0,1]
	global_store_dword v[72:73], v74, off offset:768
	s_and_saveexec_b64 s[8:9], s[4:5]
	s_cbranch_execz .LBB0_1765
	v_cndmask_b32_e64 v57, 0, v70, s[6:7]
	v_lshl_add_u64 v[70:71], s[10:11], 0, v[28:29]
	global_store_dword v[70:71], v57, off

; __device__ __forceinline__ float wave_sum(float v) {
; template <int PH, bool PRB = false>
; __device__ __forceinline__ void run_phase(int layer, LAS unsigned char* lds, const int wv_) {
;     ...
;                 float4 v[4]; float ss = 0.f;
; #pragma unroll
;                 for (int j = 0; j < 4; ++j) {
;                     typedef float f2_ __attribute__((ext_vector_type(2)));
;                     const u32x2 c = cc[q][j]; const f2_ a0 = __builtin_amdgcn_cvt_pk_f32_fp8((int)aa[q][j], false), a1 = __builtin_amdgcn_cvt_pk_f32_fp8((int)aa[q][j], true), b0 = __builtin_amdgcn_cvt_pk_f32_fp8((int)bb[q][j], false), b1 = __builtin_amdgcn_cvt_pk_f32_fp8((int)bb[q][j], true);
;                     constexpr float iy = 1.0f / pg8::YS8_SCALE;
;                     v[j].x = __uint_as_float(c.x << 16) + (a0[0] + b0[0]) * iy; v[j].y = __uint_as_float(c.x & 0xffff0000u) + (a0[1] + b0[1]) * iy;
;                     v[j].z = __uint_as_float(c.y << 16) + (a1[0] + b1[0]) * iy; v[j].w = __uint_as_float(c.y & 0xffff0000u) + (a1[1] + b1[1]) * iy;
;                     ss += v[j].x * v[j].x + v[j].y * v[j].y + v[j].z * v[j].z + v[j].w * v[j].w;
;                 }
;                 ss = wave_sum(ss);
;                 if (layer == DEPTH - 1) {
;                     const float rs = rsqrtf(ss * (1.0f / D) + 1e-6f); float4* o4 = (float4*)(p.out + (size_t)r * D);
; #pragma unroll
;                     for (int j = 0; j < 4; ++j) { const float4 gg = gfin[j]; float4 o; o.x = v[j].x * rs * gg.x; o.y = v[j].y * rs * gg.y; o.z = v[j].z * rs * gg.z; o.w = v[j].w * rs * gg.w; o4[lane + 64 * j] = o; }
;                 } else {
;                     rms_row_bf16(v, 1.0f, nullptr, hbo + (size_t)r * D, lane);
;                     if (!PRB) {
;                         const float rs8 = rsqrtf(ss * (1.0f / D) + 1e-6f); unsigned char* h8 = ws + WS_H + 32 * MiB + (size_t)r * D;
; #pragma unroll
;                         for (int j = 0; j < 4; ++j) { int w = __builtin_amdgcn_cvt_pk_fp8_f32(v[j].x * rs8, v[j].y * rs8, 0, false); w = __builtin_amdgcn_cvt_pk_fp8_f32(v[j].z * rs8, v[j].w * rs8, w, true); ((int*)h8)[lane + 64 * j] = w; }
;                     }
;                     if (lane < 16) sso[(size_t)r * 16 + lane] = lane == 0 ? ss : 0.f;
;                     if (lane == 0 && !PRB) ((float*)(ws + WS_MISC + MISC_RSROW))[r] = rsqrtf(ss * (1.0f / D) + 1e-6f);
.LBB0_1771:
	v_cvt_pk_f32_fp8_e32 v[40:41], v66
	v_cvt_pk_f32_fp8_sdwa v[42:43], v66 src0_sel:WORD_1
	v_cvt_pk_f32_fp8_e32 v[44:45], v67
	v_cvt_pk_f32_fp8_sdwa v[46:47], v67 src0_sel:WORD_1
	v_lshlrev_b32_e32 v48, 16, v38
	v_and_b32_e32 v49, 0xffff0000, v38
	v_pk_add_f32 v[40:41], v[40:41], v[44:45]
	v_lshlrev_b32_e32 v38, 16, v39
	v_and_b32_e32 v39, 0xffff0000, v39
	v_pk_add_f32 v[42:43], v[42:43], v[46:47]
	v_cvt_pk_f32_fp8_sdwa v[44:45], v62 src0_sel:WORD_1
	v_cvt_pk_f32_fp8_sdwa v[52:53], v63 src0_sel:WORD_1
	v_pk_fma_f32 v[38:39], v[42:43], 0.5, v[38:39] op_sel_hi:[1,0,1]
	v_cvt_pk_f32_fp8_e32 v[42:43], v62
	v_cvt_pk_f32_fp8_e32 v[46:47], v63
	v_lshlrev_b32_e32 v54, 16, v36
	v_and_b32_e32 v55, 0xffff0000, v36
	v_lshlrev_b32_e32 v36, 16, v37
	v_and_b32_e32 v37, 0xffff0000, v37
	v_pk_add_f32 v[44:45], v[44:45], v[52:53]
	v_pk_add_f32 v[42:43], v[42:43], v[46:47]
	v_pk_fma_f32 v[36:37], v[44:45], 0.5, v[36:37] op_sel_hi:[1,0,1]
	v_cvt_pk_f32_fp8_e32 v[44:45], v60
	v_cvt_pk_f32_fp8_sdwa v[46:47], v60 src0_sel:WORD_1
	v_cvt_pk_f32_fp8_e32 v[56:57], v61
	v_cvt_pk_f32_fp8_sdwa v[60:61], v61 src0_sel:WORD_1
	v_lshlrev_b32_e32 v62, 16, v34
	v_and_b32_e32 v63, 0xffff0000, v34
	v_lshlrev_b32_e32 v34, 16, v35
	v_and_b32_e32 v35, 0xffff0000, v35
	v_pk_add_f32 v[46:47], v[46:47], v[60:61]
	v_pk_add_f32 v[44:45], v[44:45], v[56:57]
	v_pk_fma_f32 v[34:35], v[46:47], 0.5, v[34:35] op_sel_hi:[1,0,1]
	v_cvt_pk_f32_fp8_e32 v[46:47], v59
	v_cvt_pk_f32_fp8_e32 v[66:67], v58
	v_pk_fma_f32 v[40:41], v[40:41], 0.5, v[48:49] op_sel_hi:[1,0,1]
	v_pk_fma_f32 v[42:43], v[42:43], 0.5, v[54:55] op_sel_hi:[1,0,1]
	v_pk_fma_f32 v[44:45], v[44:45], 0.5, v[62:63] op_sel_hi:[1,0,1]
	v_cvt_pk_f32_fp8_sdwa v[62:63], v59 src0_sel:WORD_1
	v_cvt_pk_f32_fp8_sdwa v[58:59], v58 src0_sel:WORD_1
	v_pk_mul_f32 v[48:49], v[40:41], v[40:41]
	v_pk_mul_f32 v[52:53], v[42:43], v[42:43]
	v_pk_mul_f32 v[50:51], v[38:39], v[38:39]
	v_pk_mul_f32 v[54:55], v[36:37], v[36:37]
	v_pk_mul_f32 v[56:57], v[44:45], v[44:45]
	v_add_f32_e32 v52, v52, v53
	v_add_f32_e32 v48, v48, v49
	v_pk_mul_f32 v[60:61], v[34:35], v[34:35]
	v_lshlrev_b32_e32 v68, 16, v32
	v_and_b32_e32 v69, 0xffff0000, v32
	v_pk_add_f32 v[46:47], v[46:47], v[66:67]
	v_add_f32_e32 v52, v52, v54
	v_add_f32_e32 v48, v48, v50
	v_add_f32_e32 v49, v56, v57
	v_pk_fma_f32 v[46:47], v[46:47], 0.5, v[68:69] op_sel_hi:[1,0,1]
	v_lshlrev_b32_e32 v32, 16, v33
	v_and_b32_e32 v33, 0xffff0000, v33
	v_pk_add_f32 v[58:59], v[62:63], v[58:59]
	v_add_f32_e32 v52, v55, v52
	v_add_f32_e32 v48, v51, v48
	v_add_f32_e32 v49, v49, v60
	v_pk_fma_f32 v[32:33], v[58:59], 0.5, v[32:33] op_sel_hi:[1,0,1]
	v_pk_mul_f32 v[58:59], v[46:47], v[46:47]
	v_add_f32_e32 v48, v48, v52
	v_add_f32_e32 v49, v61, v49
	v_pk_mul_f32 v[62:63], v[32:33], v[32:33]
	v_add_f32_e32 v48, v48, v49
	v_add_f32_e32 v49, v58, v59
	v_add_f32_e32 v49, v49, v62
	v_add_f32_e32 v49, v63, v49
	v_add_f32_e32 v48, v48, v49
	s_nop 1
	s_mov_b64 s[18:19], -1
	s_andn2_b64 vcc, exec, s[0:1]
	s_waitcnt lgkmcnt(0)
	v_add_f32_dpp v48, v48, v48 quad_perm:[1,0,3,2] row_mask:0xf bank_mask:0xf
	s_nop 1
	s_waitcnt lgkmcnt(0)
	v_add_f32_dpp v48, v48, v48 quad_perm:[2,3,0,1] row_mask:0xf bank_mask:0xf
	s_nop 1
	s_waitcnt lgkmcnt(0)
	v_add_f32_dpp v48, v48, v48 row_half_mirror row_mask:0xf bank_mask:0xf
	s_nop 1
	s_waitcnt lgkmcnt(0)
	v_add_f32_dpp v48, v48, v48 row_mirror row_mask:0xf bank_mask:0xf
	v_mov_b32_e32 v49, v48
	s_nop 1
	v_permlane16_swap_b32_e32 v48, v49
	s_waitcnt lgkmcnt(0)
	v_add_f32_e32 v48, v48, v49
	v_mov_b32_e32 v49, v48
	s_nop 1
	v_permlane32_swap_b32_e32 v48, v49
	v_add_f32_e32 v50, v48, v49
	v_fmamk_f32 v48, v50, 0x3a800000, v218
	v_cmp_gt_f32_e64 s[8:9], s61, v48
	v_mul_f32_e32 v49, 0x4b800000, v48
	s_cbranch_vccnz .LBB0_1777
	v_lshl_add_u64 v[54:55], s[10:11], 0, v[26:27]
	v_add_co_u32_e32 v54, vcc, s29, v54
	v_cndmask_b32_e64 v51, v48, v49, s[8:9]
	v_cvt_pk_bf16_f32 v52, v40, v41
	s_nop 0
	v_addc_co_u32_e32 v55, vcc, 0, v55, vcc
	v_rsq_f32_e32 v51, v51
	v_cvt_pk_bf16_f32 v53, v38, v39
	global_store_dwordx2 v[54:55], v[52:53], off
	v_cvt_pk_bf16_f32 v52, v42, v43
	v_cvt_pk_bf16_f32 v53, v36, v37
	global_store_dwordx2 v[54:55], v[52:53], off offset:512
	v_cvt_pk_bf16_f32 v52, v44, v45
	v_cvt_pk_bf16_f32 v53, v34, v35
	global_store_dwordx2 v[54:55], v[52:53], off offset:1024
	v_cvt_pk_bf16_f32 v52, v46, v47
	v_cvt_pk_bf16_f32 v53, v32, v33
	global_store_dwordx2 v[54:55], v[52:53], off offset:1536
	v_mul_f32_e32 v52, 0x45800000, v51
	v_cndmask_b32_e64 v51, v51, v52, s[8:9]
	v_mul_f32_e32 v52, v40, v51
	v_mul_f32_e32 v53, v41, v51
	v_mov_b32_e32 v54, v65
	v_cvt_pk_fp8_f32 v54, v52, v53
	v_mul_f32_e32 v52, v38, v51
	v_mul_f32_e32 v53, v39, v51
	s_mov_b32 s3, 0x2100000
	v_cvt_pk_fp8_f32 v54, v52, v53 op_sel:[0,0,1]
	v_lshl_add_u64 v[52:53], s[10:11], 0, v[24:25]
	v_add_co_u32_e32 v52, vcc, s3, v52
	v_mul_f32_e32 v55, v43, v51
	s_nop 0
	v_addc_co_u32_e32 v53, vcc, 0, v53, vcc
	global_store_dword v[52:53], v54, off
	v_mul_f32_e32 v54, v42, v51
	v_mov_b32_e32 v56, v65
	v_cvt_pk_fp8_f32 v56, v54, v55
	v_mul_f32_e32 v54, v36, v51
	v_mul_f32_e32 v55, v37, v51
	v_cvt_pk_fp8_f32 v56, v54, v55 op_sel:[0,0,1]
	v_mul_f32_e32 v54, v44, v51
	v_mul_f32_e32 v55, v45, v51
	global_store_dword v[52:53], v56, off offset:256
	v_mov_b32_e32 v56, v65
	v_cvt_pk_fp8_f32 v56, v54, v55
	v_mul_f32_e32 v54, v34, v51
	v_mul_f32_e32 v55, v35, v51
	v_cvt_pk_fp8_f32 v56, v54, v55 op_sel:[0,0,1]
	v_mul_f32_e32 v54, v46, v51
	v_mul_f32_e32 v55, v47, v51
	global_store_dword v[52:53], v56, off offset:512
	v_mov_b32_e32 v56, v65
	v_cvt_pk_fp8_f32 v56, v54, v55
	v_mul_f32_e32 v54, v32, v51
	v_mul_f32_e32 v55, v33, v51
	v_cvt_pk_fp8_f32 v56, v54, v55 op_sel:[0,0,1]
	global_store_dword v[52:53], v56, off offset:768
	s_and_saveexec_b64 s[8:9], s[4:5]
	s_cbranch_execz .LBB0_1774
	v_cndmask_b32_e64 v50, 0, v50, s[6:7]
	v_lshl_add_u64 v[52:53], s[10:11], 0, v[22:23]
	global_store_dword v[52:53], v50, off

; __device__ __forceinline__ float wave_sum(float v) {
;     v = xor_add<1>(v); v = xor_add<2>(v); v = xor_add<4>(v); v = xor_add<8>(v); v = xor_add<16>(v); v = xor_add<32>(v);
;     return v;
; }
; template <int PH, bool PRB = false>
; __device__ __forceinline__ void run_phase(int layer, LAS unsigned char* lds, const int wv_) {
;     ...
;             u32x2 cc[2][4]; unsigned aa[2][4], bb[2][4];
; #pragma unroll
;             for (int q = 0; q < 2; ++q) { const int r = r0 + q * NGW < S ? r0 + q * NGW : r0;
;                 const u32x2* hr = (const u32x2*)(hb + (size_t)r * D); const unsigned* y0 = (const unsigned*)((const unsigned char*)ys + (size_t)(2 * r) * D); const unsigned* y1 = (const unsigned*)((const unsigned char*)ys + (size_t)(2 * r + 1) * D);
; #pragma unroll
;                 for (int j = 0; j < 4; ++j) { cc[q][j] = hr[lane + 64 * j]; aa[q][j] = y0[lane + 64 * j]; bb[q][j] = y1[lane + 64 * j]; } }
; #pragma unroll
;             for (int q = 0; q < 2; ++q) { const int r = r0 + q * NGW; if (r < S) {
;                 float4 v[4]; float ss = 0.f;
; #pragma unroll
;                 for (int j = 0; j < 4; ++j) {
;                     typedef float f2_ __attribute__((ext_vector_type(2)));
;                     const u32x2 c = cc[q][j]; const f2_ a0 = __builtin_amdgcn_cvt_pk_f32_fp8((int)aa[q][j], false), a1 = __builtin_amdgcn_cvt_pk_f32_fp8((int)aa[q][j], true), b0 = __builtin_amdgcn_cvt_pk_f32_fp8((int)bb[q][j], false), b1 = __builtin_amdgcn_cvt_pk_f32_fp8((int)bb[q][j], true);
;                     constexpr float iy = 1.0f / pg8::YS8_SCALE;
;                     v[j].x = __uint_as_float(c.x << 16) + (a0[0] + b0[0]) * iy; v[j].y = __uint_as_float(c.x & 0xffff0000u) + (a0[1] + b0[1]) * iy;
;                     v[j].z = __uint_as_float(c.y << 16) + (a1[0] + b1[0]) * iy; v[j].w = __uint_as_float(c.y & 0xffff0000u) + (a1[1] + b1[1]) * iy;
;                     ss += v[j].x * v[j].x + v[j].y * v[j].y + v[j].z * v[j].z + v[j].w * v[j].w;
;                 }
;                 ss = wave_sum(ss);
.LBB0_1844:
	s_add_i32 s3, s90, s2
	s_cmpk_lt_i32 s3, 0x4000
	s_cselect_b64 s[18:19], -1, 0
	v_lshl_add_u64 v[56:57], s[10:11], 0, v[20:21]
	s_and_b64 s[8:9], s[18:19], exec
	s_waitcnt vmcnt(8)
	v_add_co_u32_e32 v32, vcc, s29, v56
	s_cselect_b32 s8, s3, s2
	s_ashr_i32 s13, s12, 31
	v_addc_co_u32_e32 v33, vcc, 0, v57, vcc
	s_lshl_b64 s[20:21], s[12:13], 10
	global_load_dwordx2 v[40:41], v[32:33], off
	global_load_dwordx2 v[42:43], v[32:33], off offset:1024
	global_load_dwordx2 v[50:51], v[32:33], off offset:1536
	global_load_dwordx2 v[44:45], v[32:33], off offset:512
	v_lshl_add_u64 v[32:33], v[18:19], 0, s[20:21]
	s_add_i32 s20, s12, 1
	s_ashr_i32 s21, s20, 31
	global_load_dword v92, v[32:33], off offset:768
	global_load_dword v52, v[32:33], off offset:256
	global_load_dword v72, v[32:33], off offset:512
	s_lshl_b64 s[20:21], s[20:21], 10
	global_load_dword v78, v[32:33], off
	v_lshl_add_u64 v[32:33], v[18:19], 0, s[20:21]
	global_load_dword v82, v[32:33], off
	global_load_dword v86, v[32:33], off offset:256
	global_load_dword v90, v[32:33], off offset:512
	global_load_dword v93, v[32:33], off offset:768
	s_lshl_b32 s20, s8, 1
	s_ashr_i32 s9, s8, 31
	s_ashr_i32 s21, s20, 31
	s_or_b32 s26, s20, 1
	s_lshl_b64 s[8:9], s[8:9], 11
	s_lshl_b64 s[20:21], s[20:21], 10
	s_ashr_i32 s27, s26, 31
	v_lshl_add_u64 v[32:33], v[16:17], 0, s[8:9]
	s_lshl_b64 s[8:9], s[26:27], 10
	v_lshl_add_u64 v[46:47], v[18:19], 0, s[20:21]
	global_load_dwordx2 v[38:39], v[32:33], off
	global_load_dwordx2 v[36:37], v[32:33], off offset:512
	global_load_dwordx2 v[34:35], v[32:33], off offset:1024
	s_nop 0
	global_load_dwordx2 v[32:33], v[32:33], off offset:1536
	v_lshl_add_u64 v[48:49], v[18:19], 0, s[8:9]
	global_load_dword v66, v[46:47], off
	global_load_dword v62, v[46:47], off offset:256
	global_load_dword v60, v[46:47], off offset:512
	global_load_dword v67, v[48:49], off
	global_load_dword v63, v[48:49], off offset:256
	global_load_dword v61, v[48:49], off offset:512
	global_load_dword v58, v[48:49], off offset:768
	global_load_dword v59, v[46:47], off offset:768
	s_mov_b64 s[20:21], -1
	s_and_b64 vcc, exec, s[0:1]
	s_waitcnt vmcnt(23)
	v_lshlrev_b32_e32 v46, 16, v40
	s_waitcnt vmcnt(22)
	v_lshlrev_b32_e32 v68, 16, v42
	v_and_b32_e32 v69, 0xffff0000, v42
	v_lshlrev_b32_e32 v70, 16, v43
	v_and_b32_e32 v71, 0xffff0000, v43
	v_and_b32_e32 v47, 0xffff0000, v40
	s_waitcnt vmcnt(18)
	v_cvt_pk_f32_fp8_e32 v[42:43], v52
	s_waitcnt vmcnt(17)
	v_cvt_pk_f32_fp8_e32 v[54:55], v72
	s_waitcnt vmcnt(15)
	v_cvt_pk_f32_fp8_e32 v[80:81], v82
	v_cvt_pk_f32_fp8_e32 v[76:77], v78
	s_waitcnt vmcnt(14)
	v_cvt_pk_f32_fp8_e32 v[84:85], v86
	v_cvt_pk_f32_fp8_sdwa v[78:79], v78 src0_sel:WORD_1
	v_cvt_pk_f32_fp8_sdwa v[82:83], v82 src0_sel:WORD_1
	s_waitcnt vmcnt(13)
	v_cvt_pk_f32_fp8_e32 v[88:89], v90
	v_cvt_pk_f32_fp8_sdwa v[52:53], v52 src0_sel:WORD_1
	v_cvt_pk_f32_fp8_sdwa v[72:73], v72 src0_sel:WORD_1
	v_cvt_pk_f32_fp8_sdwa v[86:87], v86 src0_sel:WORD_1
	v_cvt_pk_f32_fp8_sdwa v[90:91], v90 src0_sel:WORD_1
	v_lshlrev_b32_e32 v48, 16, v44
	v_and_b32_e32 v49, 0xffff0000, v44
	v_pk_add_f32 v[76:77], v[76:77], v[80:81]
	v_pk_add_f32 v[42:43], v[42:43], v[84:85]
	v_cvt_pk_f32_fp8_e32 v[74:75], v92
	v_pk_add_f32 v[78:79], v[78:79], v[82:83]
	v_pk_add_f32 v[82:83], v[54:55], v[88:89]
	v_pk_fma_f32 v[54:55], v[76:77], 0.5, v[46:47] op_sel_hi:[1,0,1]
	v_pk_fma_f32 v[46:47], v[42:43], 0.5, v[48:49] op_sel_hi:[1,0,1]
	s_waitcnt vmcnt(12)
	v_cvt_pk_f32_fp8_e32 v[48:49], v93
	v_lshlrev_b32_e32 v40, 16, v41
	v_and_b32_e32 v41, 0xffff0000, v41
	v_lshlrev_b32_e32 v44, 16, v45
	v_and_b32_e32 v45, 0xffff0000, v45
	v_pk_add_f32 v[80:81], v[52:53], v[86:87]
	v_pk_add_f32 v[72:73], v[72:73], v[90:91]
	v_pk_fma_f32 v[42:43], v[82:83], 0.5, v[68:69] op_sel_hi:[1,0,1]
	v_cvt_pk_f32_fp8_sdwa v[82:83], v92 src0_sel:WORD_1
	v_cvt_pk_f32_fp8_sdwa v[84:85], v93 src0_sel:WORD_1
	v_pk_fma_f32 v[52:53], v[78:79], 0.5, v[40:41] op_sel_hi:[1,0,1]
	v_pk_fma_f32 v[44:45], v[80:81], 0.5, v[44:45] op_sel_hi:[1,0,1]
	v_pk_fma_f32 v[40:41], v[72:73], 0.5, v[70:71] op_sel_hi:[1,0,1]
	v_pk_mul_f32 v[68:69], v[54:55], v[54:55]
	v_pk_mul_f32 v[72:73], v[46:47], v[46:47]
	v_pk_mul_f32 v[70:71], v[52:53], v[52:53]
	v_pk_mul_f32 v[76:77], v[44:45], v[44:45]
	v_pk_mul_f32 v[78:79], v[42:43], v[42:43]
	v_add_f32_e32 v72, v72, v73
	v_add_f32_e32 v68, v68, v69
	v_pk_mul_f32 v[80:81], v[40:41], v[40:41]
	v_lshlrev_b32_e32 v86, 16, v50
	v_and_b32_e32 v87, 0xffff0000, v50
	v_pk_add_f32 v[48:49], v[74:75], v[48:49]
	v_add_f32_e32 v72, v72, v76
	v_add_f32_e32 v68, v68, v70
	v_add_f32_e32 v69, v78, v79
	v_pk_fma_f32 v[48:49], v[48:49], 0.5, v[86:87] op_sel_hi:[1,0,1]
	v_lshlrev_b32_e32 v50, 16, v51
	v_and_b32_e32 v51, 0xffff0000, v51
	v_pk_add_f32 v[74:75], v[82:83], v[84:85]
	v_add_f32_e32 v72, v77, v72
	v_add_f32_e32 v68, v71, v68
	v_add_f32_e32 v69, v69, v80
	v_pk_fma_f32 v[50:51], v[74:75], 0.5, v[50:51] op_sel_hi:[1,0,1]
	v_pk_mul_f32 v[74:75], v[48:49], v[48:49]
	v_add_f32_e32 v68, v68, v72
	v_add_f32_e32 v69, v81, v69
	v_pk_mul_f32 v[82:83], v[50:51], v[50:51]
	v_add_f32_e32 v68, v68, v69
	v_add_f32_e32 v69, v74, v75
	v_add_f32_e32 v69, v69, v82
	v_add_f32_e32 v69, v83, v69
	v_add_f32_e32 v68, v68, v69
	s_nop 1
	s_waitcnt lgkmcnt(0)
	v_add_f32_dpp v68, v68, v68 quad_perm:[1,0,3,2] row_mask:0xf bank_mask:0xf
	s_nop 1
	s_waitcnt lgkmcnt(0)
	v_add_f32_dpp v68, v68, v68 quad_perm:[2,3,0,1] row_mask:0xf bank_mask:0xf
	s_nop 1
	s_waitcnt lgkmcnt(0)
	v_add_f32_dpp v68, v68, v68 row_half_mirror row_mask:0xf bank_mask:0xf
	s_nop 1
	s_waitcnt lgkmcnt(0)
	v_add_f32_dpp v68, v68, v68 row_mirror row_mask:0xf bank_mask:0xf
	v_mov_b32_e32 v69, v68
	s_nop 1
	v_permlane16_swap_b32_e32 v68, v69
	s_waitcnt lgkmcnt(0)
	v_add_f32_e32 v68, v68, v69
	v_mov_b32_e32 v69, v68
	s_nop 1
	v_permlane32_swap_b32_e32 v68, v69
	v_add_f32_e32 v70, v68, v69
	v_fmamk_f32 v68, v70, 0x3a800000, v218
	v_cmp_gt_f32_e64 s[8:9], s61, v68
	v_mul_f32_e32 v69, 0x4b800000, v68
	s_cbranch_vccz .LBB0_1851
; template <int PH, bool PRB = false>
; __device__ __forceinline__ void run_phase(int layer, LAS unsigned char* lds, const int wv_) {
;     ...
;                 } else {
;                     rms_row_bf16(v, 1.0f, nullptr, hbo + (size_t)r * D, lane);
;                     if (!PRB) {
;                         const float rs8 = rsqrtf(ss * (1.0f / D) + 1e-6f); unsigned char* h8 = ws + WS_H + 32 * MiB + (size_t)r * D;
; #pragma unroll
;                         for (int j = 0; j < 4; ++j) { int w = __builtin_amdgcn_cvt_pk_fp8_f32(v[j].x * rs8, v[j].y * rs8, 0, false); w = __builtin_amdgcn_cvt_pk_fp8_f32(v[j].z * rs8, v[j].w * rs8, w, true); ((int*)h8)[lane + 64 * j] = w; }
;                     }
;                     if (lane < 16) sso[(size_t)r * 16 + lane] = lane == 0 ? ss : 0.f;
;                     if (lane == 0 && !PRB) ((float*)(ws + WS_MISC + MISC_RSROW))[r] = rsqrtf(ss * (1.0f / D) + 1e-6f);
	s_mov_b64 s[20:21], 0x4100000
	v_lshl_add_u64 v[72:73], v[56:57], 0, s[20:21]
	s_mov_b64 s[20:21], 0x4100600
	v_lshl_add_u64 v[74:75], v[56:57], 0, s[20:21]
	s_mov_b64 s[20:21], 0x4100400
	v_lshl_add_u64 v[76:77], v[56:57], 0, s[20:21]
	s_mov_b64 s[20:21], 0x4100200
	v_lshl_add_u64 v[56:57], v[56:57], 0, s[20:21]
	v_cvt_pk_bf16_f32 v78, v54, v55
	v_cvt_pk_bf16_f32 v79, v52, v53
	global_store_dwordx2 v[72:73], v[78:79], off
	v_cvt_pk_bf16_f32 v72, v46, v47
	v_cvt_pk_bf16_f32 v73, v44, v45
	global_store_dwordx2 v[56:57], v[72:73], off
	v_cvt_pk_bf16_f32 v56, v42, v43
	v_cvt_pk_bf16_f32 v57, v40, v41
	global_store_dwordx2 v[76:77], v[56:57], off
	v_cvt_pk_bf16_f32 v56, v48, v49
	v_cvt_pk_bf16_f32 v57, v50, v51
	global_store_dwordx2 v[74:75], v[56:57], off
	v_cndmask_b32_e64 v56, v68, v69, s[8:9]
	v_rsq_f32_e32 v56, v56
	v_mov_b32_e32 v74, v65
	v_lshl_add_u64 v[72:73], s[10:11], 0, v[30:31]
	s_mov_b32 s3, 0x2100000
	v_mul_f32_e32 v57, 0x45800000, v56
	v_cndmask_b32_e64 v56, v56, v57, s[8:9]
	v_mul_f32_e32 v57, v54, v56
	v_mul_f32_e32 v71, v55, v56
	v_cvt_pk_fp8_f32 v74, v57, v71
	v_mul_f32_e32 v57, v52, v56
	v_mul_f32_e32 v71, v53, v56
	v_add_co_u32_e32 v72, vcc, s3, v72
	v_cvt_pk_fp8_f32 v74, v57, v71 op_sel:[0,0,1]
	s_nop 0
	v_addc_co_u32_e32 v73, vcc, 0, v73, vcc
	v_mul_f32_e32 v57, v46, v56
	global_store_dword v[72:73], v74, off
	v_mul_f32_e32 v71, v47, v56
	v_mov_b32_e32 v74, v65
	v_cvt_pk_fp8_f32 v74, v57, v71
	v_mul_f32_e32 v57, v44, v56
	v_mul_f32_e32 v71, v45, v56
	v_cvt_pk_fp8_f32 v74, v57, v71 op_sel:[0,0,1]
	v_mul_f32_e32 v57, v42, v56
	v_mul_f32_e32 v71, v43, v56
	global_store_dword v[72:73], v74, off offset:256
	v_mov_b32_e32 v74, v65
	v_cvt_pk_fp8_f32 v74, v57, v71
	v_mul_f32_e32 v57, v40, v56
	v_mul_f32_e32 v71, v41, v56
	v_cvt_pk_fp8_f32 v74, v57, v71 op_sel:[0,0,1]
	v_mul_f32_e32 v57, v48, v56
	v_mul_f32_e32 v71, v49, v56
	global_store_dword v[72:73], v74, off offset:512
	v_mov_b32_e32 v74, v65
	v_cvt_pk_fp8_f32 v74, v57, v71
	v_mul_f32_e32 v57, v50, v56
	v_mul_f32_e32 v71, v51, v56
	v_cvt_pk_fp8_f32 v74, v57, v71 op_sel:[0,0,1]
	global_store_dword v[72:73], v74, off offset:768
	s_and_saveexec_b64 s[8:9], s[4:5]
	s_cbranch_execz .LBB0_1847
	v_cndmask_b32_e64 v57, 0, v70, s[6:7]
	v_lshl_add_u64 v[70:71], s[10:11], 0, v[28:29]
	global_store_dword v[70:71], v57, off

; __device__ __forceinline__ float wave_sum(float v) {
; template <int PH, bool PRB = false>
; __device__ __forceinline__ void run_phase(int layer, LAS unsigned char* lds, const int wv_) {
;     ...
;                 float4 v[4]; float ss = 0.f;
; #pragma unroll
;                 for (int j = 0; j < 4; ++j) {
;                     typedef float f2_ __attribute__((ext_vector_type(2)));
;                     const u32x2 c = cc[q][j]; const f2_ a0 = __builtin_amdgcn_cvt_pk_f32_fp8((int)aa[q][j], false), a1 = __builtin_amdgcn_cvt_pk_f32_fp8((int)aa[q][j], true), b0 = __builtin_amdgcn_cvt_pk_f32_fp8((int)bb[q][j], false), b1 = __builtin_amdgcn_cvt_pk_f32_fp8((int)bb[q][j], true);
;                     constexpr float iy = 1.0f / pg8::YS8_SCALE;
;                     v[j].x = __uint_as_float(c.x << 16) + (a0[0] + b0[0]) * iy; v[j].y = __uint_as_float(c.x & 0xffff0000u) + (a0[1] + b0[1]) * iy;
;                     v[j].z = __uint_as_float(c.y << 16) + (a1[0] + b1[0]) * iy; v[j].w = __uint_as_float(c.y & 0xffff0000u) + (a1[1] + b1[1]) * iy;
;                     ss += v[j].x * v[j].x + v[j].y * v[j].y + v[j].z * v[j].z + v[j].w * v[j].w;
;                 }
;                 ss = wave_sum(ss);
;                 if (layer == DEPTH - 1) {
;                     const float rs = rsqrtf(ss * (1.0f / D) + 1e-6f); float4* o4 = (float4*)(p.out + (size_t)r * D);
; #pragma unroll
;                     for (int j = 0; j < 4; ++j) { const float4 gg = gfin[j]; float4 o; o.x = v[j].x * rs * gg.x; o.y = v[j].y * rs * gg.y; o.z = v[j].z * rs * gg.z; o.w = v[j].w * rs * gg.w; o4[lane + 64 * j] = o; }
;                 } else {
;                     rms_row_bf16(v, 1.0f, nullptr, hbo + (size_t)r * D, lane);
;                     if (!PRB) {
;                         const float rs8 = rsqrtf(ss * (1.0f / D) + 1e-6f); unsigned char* h8 = ws + WS_H + 32 * MiB + (size_t)r * D;
; #pragma unroll
;                         for (int j = 0; j < 4; ++j) { int w = __builtin_amdgcn_cvt_pk_fp8_f32(v[j].x * rs8, v[j].y * rs8, 0, false); w = __builtin_amdgcn_cvt_pk_fp8_f32(v[j].z * rs8, v[j].w * rs8, w, true); ((int*)h8)[lane + 64 * j] = w; }
;                     }
;                     if (lane < 16) sso[(size_t)r * 16 + lane] = lane == 0 ? ss : 0.f;
;                     if (lane == 0 && !PRB) ((float*)(ws + WS_MISC + MISC_RSROW))[r] = rsqrtf(ss * (1.0f / D) + 1e-6f);
.LBB0_1853:
	s_waitcnt vmcnt(7)
	v_cvt_pk_f32_fp8_e32 v[40:41], v66
	v_cvt_pk_f32_fp8_sdwa v[42:43], v66 src0_sel:WORD_1
	s_waitcnt vmcnt(4)
	v_cvt_pk_f32_fp8_e32 v[44:45], v67
	v_cvt_pk_f32_fp8_sdwa v[46:47], v67 src0_sel:WORD_1
	v_lshlrev_b32_e32 v48, 16, v38
	v_and_b32_e32 v49, 0xffff0000, v38
	v_pk_add_f32 v[40:41], v[40:41], v[44:45]
	v_lshlrev_b32_e32 v38, 16, v39
	v_and_b32_e32 v39, 0xffff0000, v39
	v_pk_add_f32 v[42:43], v[42:43], v[46:47]
	v_cvt_pk_f32_fp8_sdwa v[44:45], v62 src0_sel:WORD_1
	s_waitcnt vmcnt(3)
	v_cvt_pk_f32_fp8_sdwa v[52:53], v63 src0_sel:WORD_1
	v_pk_fma_f32 v[38:39], v[42:43], 0.5, v[38:39] op_sel_hi:[1,0,1]
	v_cvt_pk_f32_fp8_e32 v[42:43], v62
	v_cvt_pk_f32_fp8_e32 v[46:47], v63
	v_lshlrev_b32_e32 v54, 16, v36
	v_and_b32_e32 v55, 0xffff0000, v36
	v_lshlrev_b32_e32 v36, 16, v37
	v_and_b32_e32 v37, 0xffff0000, v37
	v_pk_add_f32 v[44:45], v[44:45], v[52:53]
	v_pk_add_f32 v[42:43], v[42:43], v[46:47]
	v_pk_fma_f32 v[36:37], v[44:45], 0.5, v[36:37] op_sel_hi:[1,0,1]
	v_cvt_pk_f32_fp8_e32 v[44:45], v60
	v_cvt_pk_f32_fp8_sdwa v[46:47], v60 src0_sel:WORD_1
	s_waitcnt vmcnt(2)
	v_cvt_pk_f32_fp8_e32 v[56:57], v61
	v_cvt_pk_f32_fp8_sdwa v[60:61], v61 src0_sel:WORD_1
	v_lshlrev_b32_e32 v62, 16, v34
	v_and_b32_e32 v63, 0xffff0000, v34
	v_lshlrev_b32_e32 v34, 16, v35
	v_and_b32_e32 v35, 0xffff0000, v35
	v_pk_add_f32 v[46:47], v[46:47], v[60:61]
	v_pk_add_f32 v[44:45], v[44:45], v[56:57]
	v_pk_fma_f32 v[34:35], v[46:47], 0.5, v[34:35] op_sel_hi:[1,0,1]
	s_waitcnt vmcnt(0)
	v_cvt_pk_f32_fp8_e32 v[46:47], v59
	v_cvt_pk_f32_fp8_e32 v[66:67], v58
	v_pk_fma_f32 v[40:41], v[40:41], 0.5, v[48:49] op_sel_hi:[1,0,1]
	v_pk_fma_f32 v[42:43], v[42:43], 0.5, v[54:55] op_sel_hi:[1,0,1]
	v_pk_fma_f32 v[44:45], v[44:45], 0.5, v[62:63] op_sel_hi:[1,0,1]
	v_cvt_pk_f32_fp8_sdwa v[62:63], v59 src0_sel:WORD_1
	v_cvt_pk_f32_fp8_sdwa v[58:59], v58 src0_sel:WORD_1
	v_pk_mul_f32 v[48:49], v[40:41], v[40:41]
	v_pk_mul_f32 v[52:53], v[42:43], v[42:43]
	v_pk_mul_f32 v[50:51], v[38:39], v[38:39]
	v_pk_mul_f32 v[54:55], v[36:37], v[36:37]
	v_pk_mul_f32 v[56:57], v[44:45], v[44:45]
	v_add_f32_e32 v52, v52, v53
	v_add_f32_e32 v48, v48, v49
	v_pk_mul_f32 v[60:61], v[34:35], v[34:35]
	v_lshlrev_b32_e32 v68, 16, v32
	v_and_b32_e32 v69, 0xffff0000, v32
	v_pk_add_f32 v[46:47], v[46:47], v[66:67]
	v_add_f32_e32 v52, v52, v54
	v_add_f32_e32 v48, v48, v50
	v_add_f32_e32 v49, v56, v57
	v_pk_fma_f32 v[46:47], v[46:47], 0.5, v[68:69] op_sel_hi:[1,0,1]
	v_lshlrev_b32_e32 v32, 16, v33
	v_and_b32_e32 v33, 0xffff0000, v33
	v_pk_add_f32 v[58:59], v[62:63], v[58:59]
	v_add_f32_e32 v52, v55, v52
	v_add_f32_e32 v48, v51, v48
	v_add_f32_e32 v49, v49, v60
	v_pk_fma_f32 v[32:33], v[58:59], 0.5, v[32:33] op_sel_hi:[1,0,1]
	v_pk_mul_f32 v[58:59], v[46:47], v[46:47]
	v_add_f32_e32 v48, v48, v52
	v_add_f32_e32 v49, v61, v49
	v_pk_mul_f32 v[62:63], v[32:33], v[32:33]
	v_add_f32_e32 v48, v48, v49
	v_add_f32_e32 v49, v58, v59
	v_add_f32_e32 v49, v49, v62
	v_add_f32_e32 v49, v63, v49
	v_add_f32_e32 v48, v48, v49
	s_nop 1
	s_mov_b64 s[18:19], -1
	s_andn2_b64 vcc, exec, s[0:1]
	s_waitcnt lgkmcnt(0)
	v_add_f32_dpp v48, v48, v48 quad_perm:[1,0,3,2] row_mask:0xf bank_mask:0xf
	s_nop 1
	s_waitcnt lgkmcnt(0)
	v_add_f32_dpp v48, v48, v48 quad_perm:[2,3,0,1] row_mask:0xf bank_mask:0xf
	s_nop 1
	s_waitcnt lgkmcnt(0)
	v_add_f32_dpp v48, v48, v48 row_half_mirror row_mask:0xf bank_mask:0xf
	s_nop 1
	s_waitcnt lgkmcnt(0)
	v_add_f32_dpp v48, v48, v48 row_mirror row_mask:0xf bank_mask:0xf
	v_mov_b32_e32 v49, v48
	s_nop 1
	v_permlane16_swap_b32_e32 v48, v49
	s_waitcnt lgkmcnt(0)
	v_add_f32_e32 v48, v48, v49
	v_mov_b32_e32 v49, v48
	s_nop 1
	v_permlane32_swap_b32_e32 v48, v49
	v_add_f32_e32 v50, v48, v49
	v_fmamk_f32 v48, v50, 0x3a800000, v218
	v_cmp_gt_f32_e64 s[8:9], s61, v48
	v_mul_f32_e32 v49, 0x4b800000, v48
	s_cbranch_vccnz .LBB0_1859
	v_lshl_add_u64 v[54:55], s[10:11], 0, v[26:27]
	v_add_co_u32_e32 v54, vcc, s29, v54
	v_cndmask_b32_e64 v51, v48, v49, s[8:9]
	v_cvt_pk_bf16_f32 v52, v40, v41
	s_nop 0
	v_addc_co_u32_e32 v55, vcc, 0, v55, vcc
	v_rsq_f32_e32 v51, v51
	v_cvt_pk_bf16_f32 v53, v38, v39
	global_store_dwordx2 v[54:55], v[52:53], off
	v_cvt_pk_bf16_f32 v52, v42, v43
	v_cvt_pk_bf16_f32 v53, v36, v37
	global_store_dwordx2 v[54:55], v[52:53], off offset:512
	v_cvt_pk_bf16_f32 v52, v44, v45
	v_cvt_pk_bf16_f32 v53, v34, v35
	global_store_dwordx2 v[54:55], v[52:53], off offset:1024
	v_cvt_pk_bf16_f32 v52, v46, v47
	v_cvt_pk_bf16_f32 v53, v32, v33
	global_store_dwordx2 v[54:55], v[52:53], off offset:1536
	v_mul_f32_e32 v52, 0x45800000, v51
	v_cndmask_b32_e64 v51, v51, v52, s[8:9]
	v_mul_f32_e32 v52, v40, v51
	v_mul_f32_e32 v53, v41, v51
	v_mov_b32_e32 v54, v65
	v_cvt_pk_fp8_f32 v54, v52, v53
	v_mul_f32_e32 v52, v38, v51
	v_mul_f32_e32 v53, v39, v51
	s_mov_b32 s3, 0x2100000
	v_cvt_pk_fp8_f32 v54, v52, v53 op_sel:[0,0,1]
	v_lshl_add_u64 v[52:53], s[10:11], 0, v[24:25]
	v_add_co_u32_e32 v52, vcc, s3, v52
	v_mul_f32_e32 v55, v43, v51
	s_nop 0
	v_addc_co_u32_e32 v53, vcc, 0, v53, vcc
	global_store_dword v[52:53], v54, off
	v_mul_f32_e32 v54, v42, v51
	v_mov_b32_e32 v56, v65
	v_cvt_pk_fp8_f32 v56, v54, v55
	v_mul_f32_e32 v54, v36, v51
	v_mul_f32_e32 v55, v37, v51
	v_cvt_pk_fp8_f32 v56, v54, v55 op_sel:[0,0,1]
	v_mul_f32_e32 v54, v44, v51
	v_mul_f32_e32 v55, v45, v51
	global_store_dword v[52:53], v56, off offset:256
	v_mov_b32_e32 v56, v65
	v_cvt_pk_fp8_f32 v56, v54, v55
	v_mul_f32_e32 v54, v34, v51
	v_mul_f32_e32 v55, v35, v51
	v_cvt_pk_fp8_f32 v56, v54, v55 op_sel:[0,0,1]
	v_mul_f32_e32 v54, v46, v51
	v_mul_f32_e32 v55, v47, v51
	global_store_dword v[52:53], v56, off offset:512
	v_mov_b32_e32 v56, v65
	v_cvt_pk_fp8_f32 v56, v54, v55
	v_mul_f32_e32 v54, v32, v51
	v_mul_f32_e32 v55, v33, v51
	v_cvt_pk_fp8_f32 v56, v54, v55 op_sel:[0,0,1]
	global_store_dword v[52:53], v56, off offset:768
	s_and_saveexec_b64 s[8:9], s[4:5]
	s_cbranch_execz .LBB0_1856
	v_cndmask_b32_e64 v50, 0, v50, s[6:7]
	v_lshl_add_u64 v[52:53], s[10:11], 0, v[22:23]
	global_store_dword v[52:53], v50, off
